# baseline (speedup 1.0000x reference)
.LBB3_35:
	s_or_b64 exec, exec, s[0:1]
	s_lshl_b32 s0, s21, 12
	v_lshl_or_b32 v9, v2, 2, s0
	ds_write2st64_b32 v9, v0, v1 offset1:1
	ds_write2st64_b32 v9, v3, v4 offset0:2 offset1:3
	ds_write2st64_b32 v9, v5, v6 offset0:4 offset1:5
	ds_write2st64_b32 v9, v7, v8 offset0:6 offset1:7
	v_lshl_or_b32 v0, v2, 5, s0
	ds_read_b128 v[4:7], v0
	ds_read_b128 v[8:11], v0 offset:16
	s_movk_i32 s0, 0x3f0
	s_waitcnt lgkmcnt(1)
	v_cmp_gt_f32_e32 vcc, v5, v4
	s_nop 1
	v_cndmask_b32_e32 v1, v4, v5, vcc
	v_cndmask_b32_e64 v0, 0, 1, vcc
	v_cmp_gt_f32_e32 vcc, v6, v1
	v_and_b32_e32 v5, 1, v2
	v_lshlrev_b32_e32 v4, 3, v5
	v_cndmask_b32_e32 v1, v1, v6, vcc
	v_cndmask_b32_e64 v0, v0, 2, vcc
	v_cmp_gt_f32_e32 vcc, v7, v1
	s_nop 1
	v_cndmask_b32_e32 v1, v1, v7, vcc
	v_cndmask_b32_e64 v0, v0, 3, vcc
	s_waitcnt lgkmcnt(0)
	v_cmp_gt_f32_e32 vcc, v8, v1
	s_nop 1
	v_cndmask_b32_e32 v1, v1, v8, vcc
	v_cndmask_b32_e64 v0, v0, 4, vcc
	v_cmp_gt_f32_e32 vcc, v9, v1
	s_nop 1
	v_cndmask_b32_e32 v1, v1, v9, vcc
	v_cndmask_b32_e64 v0, v0, 5, vcc
	v_cmp_gt_f32_e32 vcc, v10, v1
	s_nop 1
	v_cndmask_b32_e32 v1, v1, v10, vcc
	v_cndmask_b32_e64 v0, v0, 6, vcc
	v_cmp_gt_f32_e32 vcc, v11, v1
	s_nop 1
	v_cndmask_b32_e32 v1, v1, v11, vcc
	v_cndmask_b32_e64 v3, v0, 7, vcc
	v_and_b32_e32 v0, 0xffffffc0, v1
	v_lshlrev_b32_e32 v1, 4, v1
	v_and_or_b32 v1, v1, s0, v4
	v_add_u32_e32 v1, v1, v3
	s_nop 1
	v_mov_b32_dpp v3, v0 quad_perm:[1,0,3,2] row_mask:0xf bank_mask:0xf
	v_mov_b32_dpp v4, v1 quad_perm:[1,0,3,2] row_mask:0xf bank_mask:0xf
	v_cmp_eq_u32_e32 vcc, 0, v5
	s_and_saveexec_b64 s[0:1], vcc
	s_cbranch_execz .LBB3_37
	s_waitcnt lgkmcnt(1)
	v_cmp_eq_f32_e64 s[0:1], v3, v0
	s_waitcnt lgkmcnt(0)
	v_cmp_lt_i32_e64 s[2:3], v4, v1
	v_cmp_gt_f32_e32 vcc, v3, v0
	s_and_b64 s[0:1], s[0:1], s[2:3]
	s_or_b64 vcc, vcc, s[0:1]
	v_lshlrev_b32_e32 v5, 1, v2
	v_cndmask_b32_e32 v4, v1, v4, vcc
	v_lshrrev_b32_e32 v1, 1, v2
	v_and_b32_e32 v5, 12, v5
	v_cndmask_b32_e32 v0, v0, v3, vcc
	v_and_or_b32 v5, v1, 48, v5
	v_bfe_u32 v2, v2, 3, 2
	v_bfrev_b32_e32 v1, 1
	v_cmp_lt_i32_e32 vcc, -1, v0
	v_lshl_or_b32 v2, s20, 7, v2
	v_or_b32_e32 v2, s46, v2
	v_cndmask_b32_e32 v1, -1, v1, vcc
	v_xor_b32_e32 v1, v1, v0
	v_sub_u32_e32 v0, 0, v4
	v_add_u32_e32 v0, 0x3ff, v0
	v_add_lshl_u32 v2, v2, v5, 3
	global_atomic_umax_x2 v2, v[0:1], s[4:5]
